# layer-1 expert-weight conversion moved out of P1 to after E2 of layer 0, done by the XCD groups that received one MoE unit-group fewer (static partition, they would otherwise idle at the grid barrier)
# speedup vs baseline: 1.0154x; 1.0154x over previous
; __global__ void __launch_bounds__(NWAVES * 64, 2) mk_fwd(Args args) {
;     ...
;         {
;             const int step = G * NWAVES; int it0 = CONV_EARLY + bid * NWAVES + wave;
;             ConvDesc dA, dB; f32x4 vA[16], vB[16];
;             if (it0 < NCONV_ITEMS) { CONV_DECODE(dA, it0); conv_load(vA, dA, lane); }
; #pragma unroll 1
;             for (; it0 < NCONV_ITEMS; it0 += 2 * step) {
.LBB0_399:
	s_or_b64 exec, exec, s[0:1]
	s_mov_b64 s[0:1], s[78:79]
	s_waitcnt lgkmcnt(0)
	s_barrier
	s_mov_b32 s99, 0
	s_mov_b32 s101, 0x3900
	s_mov_b32 s98, s83
	s_mov_b32 s100, s33

; __global__ void __launch_bounds__(NWAVES * 64, 2) mk_fwd(Args args) {
;     ...
;             const int step = G * NWAVES; int it0 = CONV_EARLY + bid * NWAVES + wave;
;             ConvDesc dA, dB; f32x4 vA[16], vB[16];
;             if (it0 < NCONV_ITEMS) { CONV_DECODE(dA, it0); conv_load(vA, dA, lane); }
; #pragma unroll 1
;             for (; it0 < NCONV_ITEMS; it0 += 2 * step) {
;                 const bool hasB = it0 + step < NCONV_ITEMS, hasA2 = it0 + 2 * step < NCONV_ITEMS;
;                 if (hasB) { CONV_DECODE(dB, it0 + step); conv_load(vB, dB, lane); }
;                 conv_process(vA, dA, scr, lane);
;                 if (hasA2) { CONV_DECODE(dA, it0 + 2 * step); conv_load(vA, dA, lane); }
;                 if (hasB) conv_process(vB, dB, scr, lane);
;             }
;         }
.Lconv_go:
	v_mbcnt_lo_u32_b32 v64, -1, 0
	v_mbcnt_hi_u32_b32 v64, -1, v64
	s_load_dwordx2 s[8:9], s[0:1], 0x30
	s_mov_b64 s[0:1], s[78:79]
	s_load_dwordx2 s[10:11], s[0:1], 0x40
	s_mov_b64 s[0:1], s[78:79]
	s_load_dwordx2 s[12:13], s[0:1], 0x48
	s_mov_b64 s[0:1], s[78:79]
	s_load_dwordx2 s[14:15], s[0:1], 0x50
	s_mov_b64 s[0:1], s[78:79]
	s_load_dwordx2 s[16:17], s[0:1], 0x78
	s_mov_b64 s[0:1], s[78:79]
	s_load_dwordx2 s[18:19], s[0:1], 0x80
	s_mov_b64 s[0:1], s[78:79]
	s_load_dwordx2 s[20:21], s[0:1], 0x88
	s_mov_b64 s[0:1], s[78:79]
	s_load_dwordx2 s[22:23], s[0:1], 0xa0
	s_mov_b64 s[24:25], s[78:79]
	s_mov_b64 s[26:27], s[78:79]
	v_mov_b32_e32 v0, 0x900
	v_add_co_u32_e64 v0, s[6:7], s50, v0
	s_waitcnt lgkmcnt(0)
	s_add_u32 s38, s22, 0x2000000
	s_addc_u32 s39, s23, 0
	s_mov_b64 s[22:23], s[78:79]
	s_load_dwordx2 s[22:23], s[22:23], 0xa0
	s_load_dwordx2 s[24:25], s[24:25], 0xa0
	s_load_dwordx2 s[26:27], s[26:27], 0xa0
	s_waitcnt lgkmcnt(0)
	s_add_u32 s40, s22, 0x2400000
	s_addc_u32 s41, s23, 0
	s_mov_b64 s[22:23], s[78:79]
	s_add_u32 s42, s24, 0x2600000
	s_addc_u32 s43, s25, 0
	s_load_dwordx2 s[22:23], s[22:23], 0xa0
	s_mov_b64 s[24:25], s[78:79]
	s_add_u32 s44, s26, 0x2800000
	s_addc_u32 s45, s27, 0
	s_load_dwordx2 s[24:25], s[24:25], 0xa0
	s_mov_b64 s[26:27], s[78:79]
	s_load_dwordx2 s[26:27], s[26:27], 0xa0
	s_waitcnt lgkmcnt(0)
	s_add_u32 s46, s22, 0x3100000
	s_addc_u32 s47, s23, 0
	s_add_u32 s51, s24, 0x4000000
	s_mov_b32 s0, s101
	s_addc_u32 s52, s25, 0
	v_cmp_gt_i32_e64 s[0:1], s0, v0
	s_add_u32 s53, s26, 0xc000000
	v_readfirstlane_b32 s69, v0
	s_addc_u32 s54, s27, 0
	s_and_b64 vcc, exec, s[0:1]
	s_cbranch_vccz .LBB0_408
	s_cmpk_gt_i32 s69, 0x1ff
	s_cbranch_scc0 .LBB0_409
	s_lshl_b32 s55, s69, 2
	s_lshl_b32 s22, s69, 6
	s_and_b32 s36, s22, 0x3c0
	s_and_b32 s37, s55, 0xfc0
	s_cmpk_gt_u32 s69, 0x2ff
	s_cbranch_scc0 .LBB0_410
	s_cmpk_gt_u32 s69, 0x3ff
	s_cbranch_scc0 .LBB0_411
	s_cmpk_gt_u32 s69, 0x87f
	s_cbranch_scc0 .LBB0_412
	s_andn2_b64 vcc, exec, s[6:7]
	s_cbranch_vccz .LBB0_413
	s_mul_hi_u32 s6, s50, 0xaaaaaaab
	s_lshr_b32 s6, s6, 8
	s_mul_i32 s7, s6, 0x180
	s_sub_i32 s23, s50, s7
	s_mov_b32 s7, 0
	s_lshl_b32 s22, s23, 6
	s_lshl_b64 s[30:31], s[6:7], 21
	s_lshl_b32 s56, s23, 3
	s_and_b32 s50, s22, 0x1c0
	s_cmpk_gt_u32 s23, 0x7f
	s_cbranch_scc0 .LBB0_414
	s_cmpk_gt_u32 s23, 0xff
	s_cbranch_scc0 .LBB0_415
	s_lshl_b64 s[24:25], s[6:7], 20
	s_lshl_b32 s6, s23, 2
	s_and_b32 s6, s6, 0x7c0
	s_add_i32 s28, s6, 0xfffffc00
	s_mov_b32 s29, 0
	s_lshl_b64 s[26:27], s[28:29], 12
	s_and_b32 s6, s22, 0x3c0
	s_add_u32 s7, s20, s30
	s_addc_u32 s22, s21, s31
	s_add_u32 s24, s53, s24
	s_addc_u32 s25, s54, s25
	s_add_u32 s7, s7, s26
	s_addc_u32 s22, s22, s27
	s_lshl_b32 s23, s6, 2
	s_add_u32 s26, s7, s23
	s_addc_u32 s27, s22, 0
	s_lshl_b64 s[22:23], s[28:29], 1
	s_add_u32 s24, s24, s22
	s_addc_u32 s25, s25, s23
	s_mov_b64 s[22:23], 0
	s_branch .LBB0_416
.LBB0_408:
	s_lshl_b32 s50, s98, 5
	s_andn2_b64 vcc, exec, s[0:1]
	v_lshlrev_b32_e32 v132, 2, v64
	s_cbranch_vccz .LBB0_435
	s_branch .LBB0_739

; template <class V> __device__ __forceinline__ V ntload(const V* p) { return __builtin_nontemporal_load(p); }
; __device__ __forceinline__ void conv_load(f32x4 (&v)[16], const ConvDesc& d, int lane) {
;     const float* src = d.src + (size_t)(lane >> 4) * d.ldw + (lane & 15) * 4;
; #pragma unroll
;     for (int i = 0; i < 16; ++i) v[i] = ntload((const f32x4*)(src + (size_t)(4 * i) * d.ldw));
; }
; __global__ void __launch_bounds__(NWAVES * 64, 2) mk_fwd(Args args) {
;     ...
;             if (it0 < NCONV_ITEMS) { CONV_DECODE(dA, it0); conv_load(vA, dA, lane); }
; #pragma unroll 1
;             for (; it0 < NCONV_ITEMS; it0 += 2 * step) {
;                 const bool hasB = it0 + step < NCONV_ITEMS, hasA2 = it0 + 2 * step < NCONV_ITEMS;
;                 if (hasB) { CONV_DECODE(dB, it0 + step); conv_load(vB, dB, lane); }
;                 conv_process(vA, dA, scr, lane);
.LBB0_434:
	v_ashrrev_i32_e32 v0, 4, v64
	v_ashrrev_i32_e32 v1, 31, v0
	v_mul_lo_u32 v2, s28, v1
	v_mul_lo_u32 v3, s29, v0
	v_mad_u64_u32 v[0:1], s[30:31], s28, v0, 0
	v_add3_u32 v1, v1, v2, v3
	v_lshlrev_b32_e32 v2, 4, v64
	v_lshl_add_u64 v[0:1], v[0:1], 2, s[26:27]
	v_and_b32_e32 v2, 0xf0, v2
	v_mov_b32_e32 v3, 0
	v_lshl_add_u64 v[0:1], v[0:1], 0, v[2:3]
	s_lshl_b64 s[26:27], s[28:29], 4
	s_waitcnt vmcnt(13)
	v_lshl_add_u64 v[8:9], v[0:1], 0, s[26:27]
	global_load_dwordx4 v[0:3], v[0:1], off nt
	s_nop 0
	global_load_dwordx4 v[4:7], v[8:9], off nt
	v_lshl_add_u64 v[8:9], v[8:9], 0, s[26:27]
	s_waitcnt vmcnt(13)
	v_lshl_add_u64 v[16:17], v[8:9], 0, s[26:27]
	global_load_dwordx4 v[8:11], v[8:9], off nt
	s_nop 0
	global_load_dwordx4 v[12:15], v[16:17], off nt
	v_lshl_add_u64 v[16:17], v[16:17], 0, s[26:27]
	s_waitcnt vmcnt(13)
	v_lshl_add_u64 v[24:25], v[16:17], 0, s[26:27]
	global_load_dwordx4 v[16:19], v[16:17], off nt
	s_nop 0
	global_load_dwordx4 v[20:23], v[24:25], off nt
	v_lshl_add_u64 v[24:25], v[24:25], 0, s[26:27]
	s_waitcnt vmcnt(13)
	v_lshl_add_u64 v[32:33], v[24:25], 0, s[26:27]
	s_waitcnt vmcnt(12)
	v_lshl_add_u64 v[36:37], v[32:33], 0, s[26:27]
	s_waitcnt vmcnt(11)
	v_lshl_add_u64 v[40:41], v[36:37], 0, s[26:27]
	s_waitcnt vmcnt(10)
	v_lshl_add_u64 v[44:45], v[40:41], 0, s[26:27]
	s_waitcnt vmcnt(9)
	v_lshl_add_u64 v[48:49], v[44:45], 0, s[26:27]
	s_waitcnt vmcnt(8)
	v_lshl_add_u64 v[52:53], v[48:49], 0, s[26:27]
	s_waitcnt vmcnt(7)
	v_lshl_add_u64 v[56:57], v[52:53], 0, s[26:27]
	s_waitcnt vmcnt(6)
	v_lshl_add_u64 v[60:61], v[56:57], 0, s[26:27]
	global_load_dwordx4 v[24:27], v[24:25], off nt
	s_nop 0
	global_load_dwordx4 v[28:31], v[32:33], off nt
	s_nop 0
	global_load_dwordx4 v[32:35], v[36:37], off nt
	s_nop 0
	global_load_dwordx4 v[36:39], v[40:41], off nt
	s_nop 0
	global_load_dwordx4 v[40:43], v[44:45], off nt
	s_nop 0
	global_load_dwordx4 v[44:47], v[48:49], off nt
	s_nop 0
	global_load_dwordx4 v[48:51], v[52:53], off nt
	s_nop 0
	global_load_dwordx4 v[52:55], v[56:57], off nt
	s_nop 0
	global_load_dwordx4 v[56:59], v[60:61], off nt
	v_lshl_add_u64 v[60:61], v[60:61], 0, s[26:27]
	global_load_dwordx4 v[60:63], v[60:61], off nt
	s_lshl_b32 s50, s98, 5
	s_andn2_b64 vcc, exec, s[0:1]
	v_lshlrev_b32_e32 v132, 2, v64
	s_cbranch_vccnz .LBB0_739
.LBB0_435:
	v_ashrrev_i32_e32 v134, 4, v64
	s_movk_i32 s0, 0x104
	v_ashrrev_i32_e32 v135, 3, v64
	v_lshlrev_b32_e32 v64, 3, v64
	v_and_b32_e32 v136, 60, v132
	v_mul_lo_u32 v66, v134, s0
	v_and_b32_e32 v64, 56, v64
	s_lshl_b32 s0, s85, 2
	v_lshl_add_u32 v65, v136, 2, s3
	v_mul_u32_u24_e32 v67, 0x104, v64
	v_lshlrev_b32_e32 v68, 2, v135
	s_add_i32 s0, s50, s0
	v_ashrrev_i32_e32 v133, 31, v134
	v_mov_b32_e32 v139, 0
	v_add3_u32 v137, s3, v67, v68
	v_add_u32_e32 v140, 8, v135
	v_add_u32_e32 v141, 16, v135
	v_add_u32_e32 v142, 24, v135
	v_add_u32_e32 v143, 32, v135
	v_add_u32_e32 v144, 40, v135
	v_add_u32_e32 v145, 48, v135
	v_add_u32_e32 v146, 56, v135
	s_lshl_b32 s55, s100, 4
	s_lshl_b32 s56, s100, 6
	s_add_i32 s57, s0, 0x2400
	s_lshl_b32 s58, s100, 5
	s_add_i32 s59, s2, 0x24000
	s_add_i32 s49, s49, s88
	s_lshl_b32 s60, s100, 10
	s_movk_i32 s61, 0x7f
	s_mov_b32 s3, 0
	s_movk_i32 s62, 0xff00
	s_movk_i32 s63, 0x80
	s_mov_b32 s64, 0x2aaaaaab
	s_movk_i32 s65, 0x600
	s_movk_i32 s66, 0x400
	v_lshlrev_b32_e32 v138, 1, v64
	v_add_u32_e32 v147, v65, v66
	s_branch .LBB0_439

; __global__ void __launch_bounds__(NWAVES * 64, 2) mk_fwd(Args args) {
;     ...
;             for (; it0 < NCONV_ITEMS; it0 += 2 * step) {
;                 const bool hasB = it0 + step < NCONV_ITEMS, hasA2 = it0 + 2 * step < NCONV_ITEMS;
;                 if (hasB) { CONV_DECODE(dB, it0 + step); conv_load(vB, dB, lane); }
.LBB0_438:
	s_add_i32 s69, s67, s48
	s_add_i32 s57, s57, s56
	s_add_i32 s49, s49, s60
	s_cmp_lt_i32 s69, s101
	s_cbranch_scc0 .LBB0_739
.LBB0_439:
	s_add_i32 s67, s69, s48
	s_cmp_lt_i32 s67, s101
	s_cselect_b64 s[30:31], -1, 0
	s_cmp_ge_i32 s67, s101
	s_cbranch_scc1 .LBB0_468
	s_cmpk_gt_i32 s67, 0x1ff
	s_mov_b64 s[36:37], -1
	s_cbranch_scc0 .LBB0_465
	s_cmpk_gt_u32 s67, 0x2ff
	s_cbranch_scc0 .LBB0_462
	s_cmpk_gt_u32 s67, 0x3ff
	s_cbranch_scc0 .LBB0_459
	s_cmpk_gt_u32 s67, 0x87f
	s_cbranch_scc0 .LBB0_456
	s_cmpk_gt_u32 s67, 0x8ff
	s_cbranch_scc0 .LBB0_453
	s_add_i32 s0, s67, 0xf700
	s_and_b32 s1, s0, 0xffff
	s_mul_i32 s1, s1, 0xaaab
	s_lshr_b32 s70, s1, 24
	s_mul_i32 s1, s70, 0x180
	s_sub_i32 s0, s0, s1
	s_and_b32 s22, s0, 0xffff
	s_cmpk_gt_u32 s22, 0x7f
	s_cbranch_scc0 .LBB0_450
	s_lshl_b32 s27, s70, 21
	s_cmpk_gt_u32 s22, 0xff
	s_mov_b64 s[34:35], -1
	s_cbranch_scc0 .LBB0_448
	s_and_b32 s0, s70, 0xffff
	s_add_u32 s26, s20, s27
	s_addc_u32 s28, s21, 0
	s_lshl_b32 s0, s0, 20
	s_add_u32 s34, s53, s0
	s_addc_u32 s35, s54, 0
	s_lshl_b32 s0, s22, 2
	s_and_b32 s0, s0, 0x7c0
	s_add_i32 s2, s0, 0xfffffc00
	s_lshl_b64 s[0:1], s[2:3], 12
	s_add_u32 s0, s26, s0
	s_addc_u32 s1, s28, s1
	s_lshl_b32 s26, s22, 6
	s_and_b32 s26, s26, 0x3c0
	s_lshl_b32 s28, s26, 2
	s_add_u32 s0, s0, s28
	s_addc_u32 s1, s1, 0
	s_lshl_b64 s[28:29], s[2:3], 1
	s_add_u32 s28, s34, s28
	s_addc_u32 s29, s35, s29
	s_mov_b64 s[34:35], 0

; __device__ __forceinline__ void conv_process(const f32x4 (&v)[16], const ConvDesc& d, LAS float* scr, int lane) {
;     ...
;         *(u32x4*)(d.dst + (size_t)wmap(d.code, d.nloc + n) * d.K + 8 * c) = o; }
; __global__ void __launch_bounds__(NWAVES * 64, 2) mk_fwd(Args args) {
;     ...
;                 conv_process(vA, dA, scr, lane);
;                 if (hasA2) { CONV_DECODE(dA, it0 + 2 * step); conv_load(vA, dA, lane); }
;                 if (hasB) conv_process(vB, dB, scr, lane);
.LBB0_588:
	v_mad_i64_i32 v[180:181], s[0:1], v180, s7, 0
	v_lshl_add_u64 v[180:181], v[180:181], 1, s[24:25]
	v_lshl_add_u64 v[180:181], v[180:181], 0, v[138:139]
	global_store_dwordx4 v[180:181], v[128:131], off
	s_waitcnt lgkmcnt(0)
	s_add_i32 s69, s55, s69
	s_cmp_ge_i32 s69, s101
	s_cbranch_scc1 .LBB0_617
	s_cmpk_gt_i32 s69, 0x1ff
	s_mov_b64 s[36:37], -1
	s_cbranch_scc0 .LBB0_614
	s_cmpk_gt_u32 s69, 0x2ff
	s_cbranch_scc0 .LBB0_611
	s_cmpk_gt_u32 s69, 0x3ff
	s_cbranch_scc0 .LBB0_608
	s_cmpk_gt_u32 s69, 0x87f
	s_cbranch_scc0 .LBB0_605
	s_cmpk_gt_u32 s69, 0x8ff
	s_cbranch_scc0 .LBB0_602
	s_add_i32 s0, s69, 0xf700
	s_and_b32 s1, s0, 0xffff
	s_mul_i32 s1, s1, 0xaaab
	s_lshr_b32 s71, s1, 24
	s_mul_i32 s1, s71, 0x180
	s_sub_i32 s0, s0, s1
	s_and_b32 s70, s0, 0xffff
	s_cmpk_gt_u32 s70, 0x7f
	s_cbranch_scc0 .LBB0_599
	s_lshl_b32 s7, s71, 21
	s_cmpk_gt_u32 s70, 0xff
	s_mov_b64 s[22:23], -1
	s_cbranch_scc0 .LBB0_597
	s_and_b32 s0, s71, 0xffff
	s_add_u32 s6, s20, s7
	s_addc_u32 s22, s21, 0
	s_lshl_b32 s0, s0, 20
	s_add_u32 s24, s53, s0
	s_addc_u32 s25, s54, 0
	s_lshl_b32 s0, s70, 2
	s_and_b32 s0, s0, 0x7c0
	s_add_i32 s2, s0, 0xfffffc00
	s_lshl_b64 s[0:1], s[2:3], 12
	s_add_u32 s0, s6, s0
	s_addc_u32 s1, s22, s1
	s_lshl_b32 s6, s70, 6
	s_and_b32 s6, s6, 0x3c0
	s_lshl_b32 s22, s6, 2
	s_add_u32 s0, s0, s22
	s_addc_u32 s1, s1, 0
	s_lshl_b64 s[22:23], s[2:3], 1
	s_add_u32 s24, s24, s22
	s_addc_u32 s25, s25, s23
	s_mov_b64 s[22:23], 0

; #define KIN(i) ((const float*)(GAS const float*)karg()[i])
; #define WSP(type, off) ((type*)(KWS() + (off)))
; #define CBID() (LOCAL_OK() ? ((bid & 7) * 32 + (bid >> 3)) : bid)
; __global__ void __launch_bounds__(NWAVES * 64, 2) mk_fwd(Args args) {
;     ...
;         const float* x = KIN(0); const float* norm_mix_g = KIN(2); const float* mod = WSP(float, WS_MOD); bf16_t* xn = WSP(bf16_t, WS_XN);
;         for (int w0 = (CBID() * 8 + wave) * 32; w0 < T; w0 += G * 8 * 32) {
;             const float* mb = mod + (size_t)(w0 >> 12) * 6144;
;             ModV mv; mod_load(mv, norm_mix_g, mb + 0, mb + 1024, lane);
;             RowV ring[4];
; #pragma unroll
;             for (int d = 0; d < 4; ++d) row_load(ring[d], x + (size_t)(w0 + d) * D, lane);
.LBB0_739:
	s_cmp_eq_u32 s99, 1
	s_cbranch_scc1 .Lseam5_go
	s_cmp_eq_u32 s99, 2
	s_cbranch_scc1 .Lq_done
	s_cmpk_lg_i32 s33, 0x100
	s_cselect_b64 s[0:1], -1, 0
	v_writelane_b32 v251, s0, 9
	s_and_b32 s54, s50, 0xe0
	s_mov_b64 s[8:9], s[78:79]
	v_writelane_b32 v251, s1, 10
	s_lshr_b32 s0, s83, 3
	s_add_i32 s6, s54, s0
	s_cmpk_eq_i32 s33, 0x100
	s_cselect_b64 s[2:3], -1, 0
	s_and_b64 s[0:1], s[2:3], exec
	s_cselect_b32 s0, s6, s83
	s_lshl_b32 s0, s0, 8
	s_lshl_b32 s96, s85, 5
	s_add_i32 s6, s0, s96
	s_lshl_b32 s0, s33, 8
	v_writelane_b32 v251, s0, 11
	s_cmp_gt_i32 s6, 0xffff
	s_mov_b64 s[10:11], s[78:79]
	v_writelane_b32 v251, s1, 12
	s_mov_b64 s[0:1], s[78:79]
	s_mov_b64 s[12:13], s[78:79]
	s_cbranch_scc1 .LBB0_754
	s_load_dwordx2 s[14:15], s[10:11], 0xa0
	s_load_dwordx2 s[16:17], s[0:1], 0x0
	s_load_dwordx2 s[20:21], s[8:9], 0x10
	s_load_dwordx2 s[22:23], s[12:13], 0xa0
	v_ashrrev_i32_e32 v133, 31, v132
	s_waitcnt vmcnt(15)
	v_lshlrev_b64 v[0:1], 2, v[132:133]
	s_waitcnt lgkmcnt(0)
	s_add_u32 s18, s14, 0x100000
	v_lshl_add_u64 v[96:97], s[20:21], 0, v[0:1]
	v_lshl_add_u64 v[98:99], s[16:17], 0, v[0:1]
	v_lshlrev_b64 v[0:1], 1, v[132:133]
	s_addc_u32 s19, s15, 0
	v_lshl_add_u64 v[2:3], s[22:23], 0, v[0:1]
	s_mov_b64 s[0:1], 0x10000000
	s_ashr_i32 s7, s6, 31
	v_lshl_add_u64 v[100:101], v[2:3], 0, s[0:1]
	s_lshl_b64 s[0:1], s[6:7], 11
	s_add_u32 s0, s22, s0
	s_addc_u32 s1, s23, s1
	v_lshl_add_u64 v[0:1], s[0:1], 0, v[0:1]
	s_mov_b64 s[0:1], 0x10000400
	v_lshl_add_u64 v[102:103], v[0:1], 0, s[0:1]
	v_readlane_b32 s0, v251, 11
	v_readlane_b32 s1, v251, 12
	s_mov_b32 s8, s0
	s_ashr_i32 s9, s0, 31
	v_writelane_b32 v251, s0, 11
	s_lshl_b64 s[8:9], s[8:9], 11
	s_mov_b64 s[10:11], 0x1000
	v_mov_b32_e32 v122, 0x358637bd
	s_mov_b64 s[12:13], 0x2000
	v_writelane_b32 v251, s1, 12
	s_branch .LBB0_742

; #define KIN(i) ((const float*)(GAS const float*)karg()[i])
; #define KOUT() ((float*)(GAS float*)karg()[19])
; #define KWS() ((unsigned char*)(GAS unsigned char*)karg()[20])
; #define WSP(type, off) ((type*)(KWS() + (off)))
; #define CBID() (LOCAL_OK() ? ((bid & 7) * 32 + (bid >> 3)) : bid)
; #define SEAM(k) do { if (IN(k) && IN((k) + 1)) GRID_BAR(); } while (0)
; #define MODL() (WSP(float, WS_MOD) + (size_t)l * 16 * 6144)
; #define CNTL() (WSP(int, WS_CTL) + 64 * l)
; #define MODL() (WSP(float, WS_MOD) + (size_t)l * 16 * 6144)
; #define CNTL() (WSP(int, WS_CTL) + 64 * l)
; __global__ void __launch_bounds__(NWAVES * 64, 2) mk_fwd(Args args) {
;     ...
;         if (IN(pb0)) rt::router_phase(lds, (const bf16_t*)KOUT(), WSP(bf16_t, WS_XN), KIN(3) + l * D, MODL(), KIN(11) + (size_t)l * D * 4, KIN(12) + l * 4, KIN(13) + (size_t)l * 4 * D * 8, KIN(14) + l * 32,
;                                       CNTL(), WSP(int, WS_LTOK), WSP(float, WS_LW), WSP(int, WS_TSLOT), CBID(), G, wave, LOCAL_OK() ? (const unsigned char*)(KWS() + WS_RTAB + (size_t)l * 16 * RTAB_STRIDE) : nullptr);
;         SEAM(pb0);
.LBB0_1380:
	s_bitcmp1_b32 s83, 2
	s_cbranch_scc0 .Lseam5_go
	s_mov_b32 s99, 1
	s_mov_b32 s101, 0x3900
	s_mov_b32 s98, s83
	s_mov_b32 s100, s33
	s_lshl_b32 s48, s33, 3
	s_lshl_b32 s50, s83, 3
	s_add_i32 s50, s50, s85
	s_mov_b64 s[0:1], s[78:79]
	s_lshl_b32 s2, s33, 9
	s_mul_i32 s3, s85, 0x4100
	s_lshl_b32 s49, s83, 9
	s_lshl_b32 s88, s85, 6
	s_branch .Lconv_entry

; #define WSP(type, off) ((type*)(KWS() + (off)))
; #define SEAM(k) do { if (IN(k) && IN((k) + 1)) GRID_BAR(); } while (0)
;     __device__ bool next(int i, Unit& u) const {
;     ...
;         if (aligned) {
;             const int ng = (nM + WGM - 1) / WGM, gq = ng / NXCD, gr = ng % NXCD, xcd = (int)(L % NXCD); const long off = L / NXCD;
;             const int g0 = xcd * gq + (xcd < gr ? xcd : gr), g1 = g0 + gq + (xcd < gr ? 1 : 0);
;             const long w = (long)g0 * (WGM * 4) + off, wend = (long)g1 * (WGM * 4) < nwg ? (long)g1 * (WGM * 4) : nwg;
;             if (w >= wend) return false;
;             wgid = (int)w;
; __global__ void __launch_bounds__(NWAVES * 64, 2) mk_fwd(Args args) {
;     ...
;         for (int rep_ = 0; rep_ < REPS(7); ++rep_) if (IN(pb0 + 2)) { bf16_t* act = WSP(bf16_t, WS_ACT); bf16_t* WDN = WSP(bf16_t, WS_WDN); bf16_t* yw = WSP(bf16_t, WS_YW); const float* lw = WSP(float, WS_LW);
;             pg8::Gemm g{act, WDN + (size_t)l * 32 * 1024 * 512, 0, 0, 512}; pg8::MoeOrder S; S.init(rb[32] / 256, G, bid, rb, LOCAL_OK()); pg8::EpiDown E{yw, lw, rb};
;             pg8::gemm_phase<pg8::EpiDown, pg8::MoeOrder, pg8::APlain, true, true>(lds, g, S, E, pg8::APlain{}, wave); }
;         SEAM(pb0 + 2);
.LBB0_1657:
	s_waitcnt vmcnt(0) lgkmcnt(0)
	s_barrier
	v_mov_b32_e32 v252, 0x27c80
	ds_read_b32 v252, v252
	s_waitcnt lgkmcnt(0)
	v_readfirstlane_b32 s100, v252
	s_nop 1
	s_lshr_b32 s100, s100, 8
	s_add_i32 s100, s100, 3
	s_lshr_b32 s100, s100, 2
	s_and_b32 s100, s100, 7
	s_and_b32 s98, s83, 7
	s_cmp_eq_u32 s100, 0
	s_cbranch_scc1 .Lsp_all
	s_cmp_lt_u32 s98, s100
	s_cbranch_scc1 .Lq_done
	s_sub_i32 s98, s98, s100
	s_lshl_b32 s98, s98, 5
	s_lshr_b32 s101, s83, 3
	s_add_i32 s98, s98, s101
	s_sub_i32 s100, 8, s100
	s_lshl_b32 s100, s100, 5
	s_branch .Lsp_go
.Lsp_all:
	s_mov_b32 s98, s83
	s_mov_b32 s100, s33
.Lsp_go:
	s_add_i32 s98, s98, 0x600
	s_mov_b32 s99, 2
	s_mov_b32 s101, 0x6900
	s_lshl_b32 s50, s98, 3
	s_add_i32 s50, s50, s85
	s_lshl_b32 s49, s98, 9
	s_lshl_b32 s48, s100, 3
	s_lshl_b32 s2, s100, 9
	s_mov_b64 s[0:1], s[78:79]
	s_mul_i32 s3, s85, 0x4100
	s_lshl_b32 s88, s85, 6
	s_branch .Lconv_entry
